# v9 + gate epilogue: log2e folded into the per-row rstd (one multiply per element removed)
# speedup vs baseline: 1.0102x; 1.0012x over previous
.LBB0_2145:
	v_lshl_add_u32 v180, s24, 8, v185
	v_ashrrev_i32_e32 v181, 31, v180
	v_lshlrev_b64 v[64:65], 4, v[180:181]
	v_lshl_add_u64 v[66:67], s[8:9], 0, v[64:65]
	v_or_b32_e32 v144, 16, v180
	global_load_dwordx4 v[194:197], v[66:67], off
	v_lshl_add_u64 v[64:65], s[10:11], 0, v[64:65]
	v_ashrrev_i32_e32 v145, 31, v144
	global_load_dwordx4 v[198:201], v[64:65], off
	v_lshlrev_b64 v[64:65], 4, v[144:145]
	v_lshl_add_u64 v[66:67], s[8:9], 0, v[64:65]
	global_load_dwordx4 v[202:205], v[66:67], off
	v_lshl_add_u64 v[64:65], s[10:11], 0, v[64:65]
	v_lshl_or_b32 v182, s22, 8, v189
	global_load_dwordx4 v[206:209], v[64:65], off
	v_ashrrev_i32_e32 v183, 31, v182
	v_lshlrev_b64 v[64:65], 10, v[180:181]
	v_lshl_add_u64 v[218:219], v[64:65], 0, v[182:183]
	v_lshlrev_b64 v[64:65], 1, v[218:219]
	v_lshl_add_u64 v[146:147], s[62:63], 0, v[64:65]
	global_load_dwordx4 v[210:213], v[146:147], off
	v_lshl_add_u64 v[148:149], s[60:61], 0, v[64:65]
	global_load_dwordx4 v[214:217], v[148:149], off
	v_lshl_add_u64 v[64:65], v[182:183], 2, s[6:7]
	flat_load_dwordx4 v[76:79], v[64:65]
	flat_load_dwordx4 v[72:75], v[64:65] offset:16
	flat_load_dwordx4 v[68:71], v[64:65] offset:512
	s_nop 0
	flat_load_dwordx4 v[64:67], v[64:65] offset:528
	s_nop 0
	global_load_dwordx4 v[164:167], v[146:147], off offset:256
	global_load_dwordx4 v[160:163], v[148:149], off offset:256
	v_lshlrev_b64 v[144:145], 10, v[144:145]
	v_lshl_add_u64 v[186:187], v[144:145], 0, v[182:183]
	v_lshlrev_b64 v[144:145], 1, v[186:187]
	v_lshl_add_u64 v[146:147], s[62:63], 0, v[144:145]
	v_lshl_add_u64 v[144:145], s[60:61], 0, v[144:145]
	global_load_dwordx4 v[156:159], v[146:147], off
	global_load_dwordx4 v[148:151], v[146:147], off offset:256
	global_load_dwordx4 v[152:155], v[144:145], off
	s_nop 0
	global_load_dwordx4 v[144:147], v[144:145], off offset:256
	s_and_b64 vcc, exec, s[0:1]
	s_mov_b32 s22, s14
	s_mov_b32 s24, s16
	s_mov_b64 s[26:27], s[20:21]
	s_mov_b64 s[28:29], s[18:19]
	s_waitcnt vmcnt(0)
	v_mov_b32_e32 v220, v195
	v_mov_b32_e32 v221, v196
	v_mov_b32_e32 v195, v197
	v_mov_b32_e32 v196, v199
	v_mov_b32_e32 v197, v200
	v_mov_b32_e32 v199, v201
	v_pk_add_f32 v[194:195], v[220:221], v[194:195]
	v_pk_add_f32 v[196:197], v[196:197], v[198:199]
	v_add_f32_e32 v181, v194, v195
	v_mov_b32_e32 v198, v203
	v_mov_b32_e32 v199, v204
	v_mov_b32_e32 v203, v205
	v_add_f32_e32 v184, v196, v197
	v_fmamk_f32 v181, v181, 0x3a800000, v192
	v_pk_add_f32 v[194:195], v[198:199], v[202:203]
	v_fmamk_f32 v184, v184, 0x3a800000, v192
	v_rsq_f32_e32 v181, v181
	s_nop 0
	v_mul_f32_e32 v181, 0x3fb8aa3b, v181
	v_mov_b32_e32 v200, v207
	v_mov_b32_e32 v201, v208
	v_mov_b32_e32 v207, v209
	v_add_f32_e32 v193, v194, v195
	v_rsq_f32_e32 v194, v184
	v_pk_add_f32 v[196:197], v[200:201], v[206:207]
	v_lshlrev_b32_e32 v198, 16, v210
	v_add_f32_e32 v195, v196, v197
	v_and_b32_e32 v199, 0xffff0000, v210
	v_lshlrev_b32_e32 v202, 16, v212
	v_and_b32_e32 v203, 0xffff0000, v212
	v_fmamk_f32 v184, v195, 0x3a800000, v192
	v_mul_f32_e64 v195, v140, -v181
	v_mul_f32_e64 v196, v136, -v181
	v_mul_f32_e64 v197, v141, -v181
	v_mul_f32_e64 v206, v137, -v181
	v_pk_mul_f32 v[136:137], v[194:195], v[198:199] op_sel_hi:[0,1]
	v_pk_mul_f32 v[140:141], v[194:195], v[202:203] op_sel_hi:[0,1]
	v_mov_b32_e32 v198, v206
	v_exp_f32_e32 v195, v195
	v_exp_f32_e32 v196, v196
	v_exp_f32_e32 v198, v198
	v_mul_f32_e64 v142, v142, -v181
	v_mul_f32_e64 v138, v138, -v181
	v_exp_f32_e32 v197, v197
	v_add_f32_e32 v195, 1.0, v195
	v_add_f32_e32 v199, 1.0, v196
	v_rcp_f32_e32 v196, v195
	v_add_f32_e32 v195, 1.0, v198
	v_mul_f32_e64 v143, v143, -v181
	v_exp_f32_e32 v142, v142
	v_rcp_f32_e32 v198, v199
	v_rcp_f32_e32 v199, v195
	v_exp_f32_e32 v195, v138
	v_exp_f32_e32 v143, v143
	v_add_f32_e32 v197, 1.0, v197
	v_mul_f32_e64 v139, v139, -v181
	v_rcp_f32_e32 v197, v197
	v_add_f32_e32 v138, 1.0, v142
	v_add_f32_e32 v142, 1.0, v195
	v_exp_f32_e32 v195, v139
	v_add_f32_e32 v139, 1.0, v143
	v_lshlrev_b32_e32 v200, 16, v214
	v_and_b32_e32 v201, 0xffff0000, v214
	s_waitcnt lgkmcnt(0)
	v_pk_mul_f32 v[136:137], v[76:77], v[136:137]
	v_rcp_f32_e32 v138, v138
	v_rcp_f32_e32 v139, v139
	v_pk_fma_f32 v[136:137], v[136:137], v[196:197], v[200:201]
	v_lshlrev_b32_e32 v196, 16, v211
	v_and_b32_e32 v197, 0xffff0000, v211
	v_lshlrev_b32_e32 v204, 16, v216
	v_and_b32_e32 v205, 0xffff0000, v216
	v_pk_mul_f32 v[140:141], v[72:73], v[140:141]
	v_add_f32_e32 v143, 1.0, v195
	v_pk_mul_f32 v[196:197], v[194:195], v[196:197] op_sel_hi:[0,1]
	v_pk_fma_f32 v[140:141], v[140:141], v[198:199], v[204:205]
	v_rcp_f32_e32 v142, v142
	v_rcp_f32_e32 v143, v143
	v_lshlrev_b32_e32 v198, 16, v215
	v_and_b32_e32 v199, 0xffff0000, v215
	v_pk_mul_f32 v[196:197], v[78:79], v[196:197]
	v_mul_f32_e64 v132, v132, -v181
	v_pk_fma_f32 v[138:139], v[196:197], v[138:139], v[198:199]
	v_lshlrev_b32_e32 v196, 16, v213
	v_and_b32_e32 v197, 0xffff0000, v213
	v_pk_mul_f32 v[196:197], v[194:195], v[196:197] op_sel_hi:[0,1]
	v_lshlrev_b32_e32 v198, 16, v217
	v_and_b32_e32 v199, 0xffff0000, v217
	v_pk_mul_f32 v[196:197], v[74:75], v[196:197]
	v_mul_f32_e64 v128, v128, -v181
	v_pk_fma_f32 v[142:143], v[196:197], v[142:143], v[198:199]
	v_lshl_add_u64 v[196:197], v[218:219], 2, s[44:45]
	global_store_dwordx4 v[196:197], v[136:139], off
	v_exp_f32_e32 v132, v132
	v_mul_f32_e64 v133, v133, -v181
	v_exp_f32_e32 v136, v128
	v_exp_f32_e32 v133, v133
	v_mul_f32_e64 v129, v129, -v181
	v_add_f32_e32 v128, 1.0, v132
	v_add_f32_e32 v132, 1.0, v136
	v_exp_f32_e32 v136, v129
	v_add_f32_e32 v129, 1.0, v133
	v_rcp_f32_e32 v128, v128
	v_rcp_f32_e32 v129, v129
	v_add_f32_e32 v133, 1.0, v136
	v_lshlrev_b32_e32 v136, 16, v164
	v_and_b32_e32 v137, 0xffff0000, v164
	v_pk_mul_f32 v[136:137], v[194:195], v[136:137] op_sel_hi:[0,1]
	v_rcp_f32_e32 v132, v132
	v_rcp_f32_e32 v133, v133
	v_lshlrev_b32_e32 v138, 16, v160
	v_and_b32_e32 v139, 0xffff0000, v160
	v_pk_mul_f32 v[136:137], v[68:69], v[136:137]
	v_mul_f32_e64 v134, v134, -v181
	v_mul_f32_e64 v135, v135, -v181
	v_pk_fma_f32 v[128:129], v[136:137], v[128:129], v[138:139]
	v_lshlrev_b32_e32 v136, 16, v166
	v_and_b32_e32 v137, 0xffff0000, v166
	v_pk_mul_f32 v[136:137], v[194:195], v[136:137] op_sel_hi:[0,1]
	v_exp_f32_e32 v134, v134
	v_exp_f32_e32 v135, v135
	v_mul_f32_e64 v131, v131, -v181
	v_lshlrev_b32_e32 v138, 16, v162
	v_and_b32_e32 v139, 0xffff0000, v162
	v_pk_mul_f32 v[136:137], v[64:65], v[136:137]
	v_mul_f32_e64 v130, v130, -v181
	v_pk_fma_f32 v[132:133], v[136:137], v[132:133], v[138:139]
	v_exp_f32_e32 v136, v131
	v_fmamk_f32 v193, v193, 0x3a800000, v192
	v_rsq_f32_e32 v193, v193
	s_nop 0
	v_mul_f32_e32 v193, 0x3fb8aa3b, v193
	global_store_dwordx4 v[196:197], v[140:143], off offset:16
	v_add_f32_e32 v131, 1.0, v135
	v_rcp_f32_e32 v131, v131
	v_exp_f32_e32 v140, v130
	v_add_f32_e32 v130, 1.0, v134
	v_rcp_f32_e32 v130, v130
	v_add_f32_e32 v135, 1.0, v136
	v_lshlrev_b32_e32 v136, 16, v165
	v_and_b32_e32 v137, 0xffff0000, v165
	v_pk_mul_f32 v[136:137], v[194:195], v[136:137] op_sel_hi:[0,1]
	v_lshlrev_b32_e32 v138, 16, v161
	v_and_b32_e32 v139, 0xffff0000, v161
	v_pk_mul_f32 v[136:137], v[70:71], v[136:137]
	v_mul_f32_e64 v124, v124, -v193
	v_mul_f32_e64 v120, v120, -v193
	v_pk_fma_f32 v[130:131], v[136:137], v[130:131], v[138:139]
	global_store_dwordx4 v[196:197], v[128:131], off offset:512
	v_exp_f32_e32 v124, v124
	v_mul_f32_e64 v125, v125, -v193
	v_exp_f32_e32 v128, v120
	v_exp_f32_e32 v125, v125
	v_mul_f32_e64 v121, v121, -v193
	v_add_f32_e32 v120, 1.0, v124
	v_add_f32_e32 v124, 1.0, v128
	v_exp_f32_e32 v128, v121
	v_rsq_f32_e32 v184, v184
	v_add_f32_e32 v121, 1.0, v125
	v_rcp_f32_e32 v120, v120
	v_rcp_f32_e32 v121, v121
	v_add_f32_e32 v125, 1.0, v128
	v_lshlrev_b32_e32 v128, 16, v156
	v_and_b32_e32 v129, 0xffff0000, v156
	v_add_f32_e32 v134, 1.0, v140
	v_pk_mul_f32 v[128:129], v[184:185], v[128:129] op_sel_hi:[0,1]
	v_rcp_f32_e32 v134, v134
	v_rcp_f32_e32 v135, v135
	v_rcp_f32_e32 v124, v124
	v_rcp_f32_e32 v125, v125
	v_lshlrev_b32_e32 v130, 16, v152
	v_and_b32_e32 v131, 0xffff0000, v152
	v_pk_mul_f32 v[128:129], v[76:77], v[128:129]
	v_mul_f32_e64 v126, v126, -v193
	v_mul_f32_e64 v127, v127, -v193
	v_lshlrev_b32_e32 v136, 16, v167
	v_and_b32_e32 v137, 0xffff0000, v167
	v_pk_fma_f32 v[120:121], v[128:129], v[120:121], v[130:131]
	v_lshlrev_b32_e32 v128, 16, v158
	v_and_b32_e32 v129, 0xffff0000, v158
	v_pk_mul_f32 v[136:137], v[194:195], v[136:137] op_sel_hi:[0,1]
	v_pk_mul_f32 v[128:129], v[184:185], v[128:129] op_sel_hi:[0,1]
	v_exp_f32_e32 v126, v126
	v_exp_f32_e32 v127, v127
	v_mul_f32_e64 v123, v123, -v193
	v_lshlrev_b32_e32 v138, 16, v163
	v_and_b32_e32 v139, 0xffff0000, v163
	v_pk_mul_f32 v[136:137], v[66:67], v[136:137]
	v_lshlrev_b32_e32 v130, 16, v154
	v_and_b32_e32 v131, 0xffff0000, v154
	v_pk_mul_f32 v[128:129], v[72:73], v[128:129]
	v_mul_f32_e64 v122, v122, -v193
	v_pk_fma_f32 v[134:135], v[136:137], v[134:135], v[138:139]
	v_pk_fma_f32 v[124:125], v[128:129], v[124:125], v[130:131]
	v_exp_f32_e32 v128, v123
	global_store_dwordx4 v[196:197], v[132:135], off offset:528
	v_add_f32_e32 v123, 1.0, v127
	v_rcp_f32_e32 v123, v123
	v_exp_f32_e32 v132, v122
	v_add_f32_e32 v122, 1.0, v126
	v_rcp_f32_e32 v122, v122
	v_add_f32_e32 v127, 1.0, v128
	v_lshlrev_b32_e32 v128, 16, v157
	v_and_b32_e32 v129, 0xffff0000, v157
	v_add_f32_e32 v126, 1.0, v132
	v_pk_mul_f32 v[128:129], v[184:185], v[128:129] op_sel_hi:[0,1]
	v_rcp_f32_e32 v126, v126
	v_rcp_f32_e32 v127, v127
	v_lshlrev_b32_e32 v130, 16, v153
	v_and_b32_e32 v131, 0xffff0000, v153
	v_pk_mul_f32 v[128:129], v[78:79], v[128:129]
	v_mul_f32_e64 v116, v116, -v193
	v_pk_fma_f32 v[122:123], v[128:129], v[122:123], v[130:131]
	v_lshlrev_b32_e32 v128, 16, v159
	v_and_b32_e32 v129, 0xffff0000, v159
	v_pk_mul_f32 v[128:129], v[184:185], v[128:129] op_sel_hi:[0,1]
	v_lshlrev_b32_e32 v130, 16, v155
	v_and_b32_e32 v131, 0xffff0000, v155
	v_pk_mul_f32 v[128:129], v[74:75], v[128:129]
	v_mul_f32_e64 v112, v112, -v193
	v_pk_fma_f32 v[126:127], v[128:129], v[126:127], v[130:131]
	v_lshl_add_u64 v[128:129], v[186:187], 2, s[44:45]
	global_store_dwordx4 v[128:129], v[120:123], off
	v_exp_f32_e32 v116, v116
	v_mul_f32_e64 v117, v117, -v193
	v_exp_f32_e32 v120, v112
	v_exp_f32_e32 v117, v117
	v_mul_f32_e64 v113, v113, -v193
	v_add_f32_e32 v112, 1.0, v116
	v_add_f32_e32 v116, 1.0, v120
	v_exp_f32_e32 v120, v113
	v_add_f32_e32 v113, 1.0, v117
	v_rcp_f32_e32 v112, v112
	v_rcp_f32_e32 v113, v113
	v_add_f32_e32 v117, 1.0, v120
	v_lshlrev_b32_e32 v120, 16, v148
	v_and_b32_e32 v121, 0xffff0000, v148
	v_pk_mul_f32 v[120:121], v[184:185], v[120:121] op_sel_hi:[0,1]
	v_rcp_f32_e32 v116, v116
	v_rcp_f32_e32 v117, v117
	v_lshlrev_b32_e32 v122, 16, v144
	v_and_b32_e32 v123, 0xffff0000, v144
	v_pk_mul_f32 v[120:121], v[68:69], v[120:121]
	v_mul_f32_e64 v118, v118, -v193
	v_mul_f32_e64 v119, v119, -v193
	v_pk_fma_f32 v[112:113], v[120:121], v[112:113], v[122:123]
	v_lshlrev_b32_e32 v120, 16, v150
	v_and_b32_e32 v121, 0xffff0000, v150
	v_pk_mul_f32 v[120:121], v[184:185], v[120:121] op_sel_hi:[0,1]
	v_exp_f32_e32 v118, v118
	v_exp_f32_e32 v119, v119
	v_mul_f32_e64 v115, v115, -v193
	v_lshlrev_b32_e32 v122, 16, v146
	v_and_b32_e32 v123, 0xffff0000, v146
	v_pk_mul_f32 v[120:121], v[64:65], v[120:121]
	v_mul_f32_e64 v114, v114, -v193
	v_pk_fma_f32 v[116:117], v[120:121], v[116:117], v[122:123]
	v_exp_f32_e32 v120, v115
	global_store_dwordx4 v[128:129], v[124:127], off offset:16
	v_add_f32_e32 v115, 1.0, v119
	v_rcp_f32_e32 v115, v115
	v_exp_f32_e32 v124, v114
	v_add_f32_e32 v114, 1.0, v118
	v_rcp_f32_e32 v114, v114
	v_add_f32_e32 v119, 1.0, v120
	v_lshlrev_b32_e32 v120, 16, v149
	v_and_b32_e32 v121, 0xffff0000, v149
	v_add_f32_e32 v118, 1.0, v124
	v_pk_mul_f32 v[120:121], v[184:185], v[120:121] op_sel_hi:[0,1]
	v_rcp_f32_e32 v118, v118
	v_rcp_f32_e32 v119, v119
	v_lshlrev_b32_e32 v122, 16, v145
	v_and_b32_e32 v123, 0xffff0000, v145
	v_pk_mul_f32 v[120:121], v[70:71], v[120:121]
	v_or_b32_e32 v130, 48, v180
	v_pk_fma_f32 v[114:115], v[120:121], v[114:115], v[122:123]
	v_lshlrev_b32_e32 v120, 16, v151
	v_and_b32_e32 v121, 0xffff0000, v151
	v_pk_mul_f32 v[120:121], v[184:185], v[120:121] op_sel_hi:[0,1]
	v_lshlrev_b32_e32 v122, 16, v147
	v_and_b32_e32 v123, 0xffff0000, v147
	v_pk_mul_f32 v[120:121], v[66:67], v[120:121]
	v_ashrrev_i32_e32 v131, 31, v130
	v_pk_fma_f32 v[118:119], v[120:121], v[118:119], v[122:123]
	global_store_dwordx4 v[128:129], v[112:115], off offset:512
	global_store_dwordx4 v[128:129], v[116:119], off offset:528
	v_or_b32_e32 v128, 32, v180
	v_ashrrev_i32_e32 v129, 31, v128
	v_lshlrev_b64 v[116:117], 4, v[128:129]
	v_lshl_add_u64 v[112:113], s[8:9], 0, v[116:117]
	global_load_dwordx4 v[112:115], v[112:113], off
	v_lshl_add_u64 v[116:117], s[10:11], 0, v[116:117]
	global_load_dwordx4 v[116:119], v[116:117], off
	v_lshlrev_b64 v[124:125], 4, v[130:131]
	v_lshl_add_u64 v[120:121], s[8:9], 0, v[124:125]
	global_load_dwordx4 v[120:123], v[120:121], off
	v_lshl_add_u64 v[124:125], s[10:11], 0, v[124:125]
	global_load_dwordx4 v[124:127], v[124:125], off
	v_lshlrev_b64 v[128:129], 10, v[128:129]
	v_lshl_add_u64 v[148:149], v[128:129], 0, v[182:183]
	v_lshlrev_b64 v[128:129], 1, v[148:149]
	v_lshl_add_u64 v[140:141], s[62:63], 0, v[128:129]
	global_load_dwordx4 v[132:135], v[140:141], off
	v_lshl_add_u64 v[128:129], s[60:61], 0, v[128:129]
	global_load_dwordx4 v[136:139], v[128:129], off
	s_waitcnt vmcnt(5)
	v_mov_b32_e32 v142, v113
	v_mov_b32_e32 v143, v114
	v_mov_b32_e32 v113, v115
	v_pk_add_f32 v[112:113], v[142:143], v[112:113]
	global_load_dwordx4 v[140:143], v[140:141], off offset:256
	s_nop 0
	global_load_dwordx4 v[144:147], v[128:129], off offset:256
	v_add_f32_e32 v112, v112, v113
	v_fmamk_f32 v114, v112, 0x3a800000, v192
	s_waitcnt vmcnt(6)
	v_mov_b32_e32 v112, v117
	v_mov_b32_e32 v113, v118
	v_mov_b32_e32 v117, v119
	v_pk_add_f32 v[112:113], v[112:113], v[116:117]
	v_rsq_f32_e32 v129, v114
	s_nop 0
	v_mul_f32_e32 v129, 0x3fb8aa3b, v129
	v_add_f32_e32 v112, v112, v113
	v_fmamk_f32 v112, v112, 0x3a800000, v192
	v_rsq_f32_e32 v150, v112
	v_lshlrev_b64 v[112:113], 10, v[130:131]
	v_lshl_add_u64 v[130:131], v[112:113], 0, v[182:183]
	s_waitcnt vmcnt(5)
	v_mov_b32_e32 v112, v121
	v_mov_b32_e32 v113, v122
	v_mov_b32_e32 v121, v123
	v_pk_add_f32 v[112:113], v[112:113], v[120:121]
	v_mul_f32_e64 v108, v108, -v129
	v_add_f32_e32 v112, v112, v113
	v_fmamk_f32 v151, v112, 0x3a800000, v192
	s_waitcnt vmcnt(4)
	v_mov_b32_e32 v112, v125
	v_mov_b32_e32 v113, v126
	v_mov_b32_e32 v125, v127
	v_pk_add_f32 v[112:113], v[112:113], v[124:125]
	v_mul_f32_e64 v104, v104, -v129
	v_add_f32_e32 v112, v112, v113
	v_fmamk_f32 v112, v112, 0x3a800000, v192
	v_rsq_f32_e32 v128, v112
	v_lshlrev_b64 v[112:113], 1, v[130:131]
	v_lshl_add_u64 v[114:115], s[62:63], 0, v[112:113]
	v_lshl_add_u64 v[112:113], s[60:61], 0, v[112:113]
	global_load_dwordx4 v[124:127], v[114:115], off
	global_load_dwordx4 v[116:119], v[114:115], off offset:256
	global_load_dwordx4 v[120:123], v[112:113], off
	s_nop 0
	global_load_dwordx4 v[112:115], v[112:113], off offset:256
	v_exp_f32_e32 v108, v108
	v_exp_f32_e32 v152, v104
	v_mul_f32_e64 v109, v109, -v129
	v_mul_f32_e64 v105, v105, -v129
	v_add_f32_e32 v104, 1.0, v108
	v_add_f32_e32 v108, 1.0, v152
	v_exp_f32_e32 v109, v109
	v_exp_f32_e32 v152, v105
	v_mul_f32_e64 v110, v110, -v129
	v_mul_f32_e64 v106, v106, -v129
	v_add_f32_e32 v105, 1.0, v109
	v_add_f32_e32 v109, 1.0, v152
	s_waitcnt vmcnt(7)
	v_lshlrev_b32_e32 v152, 16, v132
	v_and_b32_e32 v153, 0xffff0000, v132
	v_exp_f32_e32 v110, v110
	v_exp_f32_e32 v132, v106
	v_mul_f32_e64 v111, v111, -v129
	v_exp_f32_e32 v111, v111
	v_mul_f32_e64 v107, v107, -v129
	v_add_f32_e32 v106, 1.0, v110
	v_add_f32_e32 v110, 1.0, v132
	v_exp_f32_e32 v132, v107
	v_rsq_f32_e32 v151, v151
	s_nop 0
	v_mul_f32_e32 v151, 0x3fb8aa3b, v151
	v_add_f32_e32 v107, 1.0, v111
	v_rcp_f32_e32 v106, v106
	v_rcp_f32_e32 v107, v107
	v_add_f32_e32 v111, 1.0, v132
	v_lshlrev_b32_e32 v132, 16, v133
	v_and_b32_e32 v133, 0xffff0000, v133
	v_rcp_f32_e32 v104, v104
	v_rcp_f32_e32 v105, v105
	v_pk_mul_f32 v[132:133], v[150:151], v[132:133] op_sel_hi:[0,1]
	s_waitcnt vmcnt(6)
	v_lshlrev_b32_e32 v154, 16, v136
	v_and_b32_e32 v155, 0xffff0000, v136
	v_rcp_f32_e32 v110, v110
	v_rcp_f32_e32 v111, v111
	v_lshlrev_b32_e32 v136, 16, v137
	v_and_b32_e32 v137, 0xffff0000, v137
	v_pk_mul_f32 v[132:133], v[78:79], v[132:133]
	v_pk_mul_f32 v[152:153], v[150:151], v[152:153] op_sel_hi:[0,1]
	v_pk_fma_f32 v[106:107], v[132:133], v[106:107], v[136:137]
	v_lshlrev_b32_e32 v132, 16, v135
	v_and_b32_e32 v133, 0xffff0000, v135
	v_pk_mul_f32 v[152:153], v[76:77], v[152:153]
	v_pk_mul_f32 v[132:133], v[150:151], v[132:133] op_sel_hi:[0,1]
	v_pk_fma_f32 v[104:105], v[152:153], v[104:105], v[154:155]
	v_lshlrev_b32_e32 v152, 16, v134
	v_and_b32_e32 v153, 0xffff0000, v134
	v_lshlrev_b32_e32 v134, 16, v139
	v_and_b32_e32 v135, 0xffff0000, v139
	v_pk_mul_f32 v[132:133], v[74:75], v[132:133]
	v_mul_f32_e64 v100, v100, -v129
	v_mul_f32_e64 v96, v96, -v129
	v_pk_fma_f32 v[110:111], v[132:133], v[110:111], v[134:135]
	v_lshl_add_u64 v[132:133], v[148:149], 2, s[44:45]
	global_store_dwordx4 v[132:133], v[104:107], off
	v_exp_f32_e32 v100, v100
	v_mul_f32_e64 v101, v101, -v129
	v_exp_f32_e32 v104, v96
	v_exp_f32_e32 v101, v101
	v_mul_f32_e64 v97, v97, -v129
	v_add_f32_e32 v96, 1.0, v100
	v_add_f32_e32 v100, 1.0, v104
	v_exp_f32_e32 v104, v97
	v_add_f32_e32 v97, 1.0, v101
	v_rcp_f32_e32 v96, v96
	v_rcp_f32_e32 v97, v97
	v_add_f32_e32 v101, 1.0, v104
	s_waitcnt vmcnt(6)
	v_lshlrev_b32_e32 v104, 16, v140
	v_and_b32_e32 v105, 0xffff0000, v140
	v_pk_mul_f32 v[104:105], v[150:151], v[104:105] op_sel_hi:[0,1]
	v_rcp_f32_e32 v100, v100
	v_rcp_f32_e32 v101, v101
	s_waitcnt vmcnt(5)
	v_lshlrev_b32_e32 v106, 16, v144
	v_and_b32_e32 v107, 0xffff0000, v144
	v_pk_mul_f32 v[104:105], v[68:69], v[104:105]
	v_mul_f32_e64 v102, v102, -v129
	v_mul_f32_e64 v103, v103, -v129
	v_rcp_f32_e32 v108, v108
	v_rcp_f32_e32 v109, v109
	v_pk_fma_f32 v[96:97], v[104:105], v[96:97], v[106:107]
	v_lshlrev_b32_e32 v104, 16, v142
	v_and_b32_e32 v105, 0xffff0000, v142
	v_pk_mul_f32 v[104:105], v[150:151], v[104:105] op_sel_hi:[0,1]
	v_exp_f32_e32 v102, v102
	v_exp_f32_e32 v103, v103
	v_mul_f32_e64 v99, v99, -v129
	v_pk_mul_f32 v[152:153], v[150:151], v[152:153] op_sel_hi:[0,1]
	v_lshlrev_b32_e32 v106, 16, v146
	v_and_b32_e32 v107, 0xffff0000, v146
	v_pk_mul_f32 v[104:105], v[64:65], v[104:105]
	v_lshlrev_b32_e32 v154, 16, v138
	v_and_b32_e32 v155, 0xffff0000, v138
	v_pk_mul_f32 v[152:153], v[72:73], v[152:153]
	v_mul_f32_e64 v98, v98, -v129
	v_pk_fma_f32 v[100:101], v[104:105], v[100:101], v[106:107]
	v_exp_f32_e32 v104, v99
	v_pk_fma_f32 v[108:109], v[152:153], v[108:109], v[154:155]
	global_store_dwordx4 v[132:133], v[108:111], off offset:16
	v_add_f32_e32 v99, 1.0, v103
	v_rcp_f32_e32 v99, v99
	v_exp_f32_e32 v108, v98
	v_add_f32_e32 v98, 1.0, v102
	v_rcp_f32_e32 v98, v98
	v_add_f32_e32 v103, 1.0, v104
	v_lshlrev_b32_e32 v104, 16, v141
	v_and_b32_e32 v105, 0xffff0000, v141
	v_pk_mul_f32 v[104:105], v[150:151], v[104:105] op_sel_hi:[0,1]
	v_lshlrev_b32_e32 v106, 16, v145
	v_and_b32_e32 v107, 0xffff0000, v145
	v_pk_mul_f32 v[104:105], v[70:71], v[104:105]
	v_mul_f32_e64 v92, v92, -v151
	v_mul_f32_e64 v88, v88, -v151
	v_pk_fma_f32 v[98:99], v[104:105], v[98:99], v[106:107]
	global_store_dwordx4 v[132:133], v[96:99], off offset:512
	v_exp_f32_e32 v92, v92
	v_mul_f32_e64 v93, v93, -v151
	v_exp_f32_e32 v96, v88
	v_exp_f32_e32 v93, v93
	v_mul_f32_e64 v89, v89, -v151
	v_add_f32_e32 v88, 1.0, v92
	v_add_f32_e32 v92, 1.0, v96
	v_exp_f32_e32 v96, v89
	v_add_f32_e32 v89, 1.0, v93
	v_rcp_f32_e32 v88, v88
	v_rcp_f32_e32 v89, v89
	v_add_f32_e32 v93, 1.0, v96
	s_waitcnt vmcnt(6)
	v_lshlrev_b32_e32 v96, 16, v124
	v_and_b32_e32 v97, 0xffff0000, v124
	v_add_f32_e32 v102, 1.0, v108
	v_pk_mul_f32 v[96:97], v[128:129], v[96:97] op_sel_hi:[0,1]
	v_rcp_f32_e32 v102, v102
	v_rcp_f32_e32 v103, v103
	v_rcp_f32_e32 v92, v92
	v_rcp_f32_e32 v93, v93
	s_waitcnt vmcnt(4)
	v_lshlrev_b32_e32 v98, 16, v120
	v_and_b32_e32 v99, 0xffff0000, v120
	v_pk_mul_f32 v[96:97], v[76:77], v[96:97]
	v_mul_f32_e64 v94, v94, -v151
	v_mul_f32_e64 v95, v95, -v151
	v_lshlrev_b32_e32 v104, 16, v143
	v_and_b32_e32 v105, 0xffff0000, v143
	v_pk_fma_f32 v[88:89], v[96:97], v[88:89], v[98:99]
	v_lshlrev_b32_e32 v96, 16, v126
	v_and_b32_e32 v97, 0xffff0000, v126
	v_pk_mul_f32 v[104:105], v[150:151], v[104:105] op_sel_hi:[0,1]
	v_pk_mul_f32 v[96:97], v[128:129], v[96:97] op_sel_hi:[0,1]
	v_exp_f32_e32 v94, v94
	v_exp_f32_e32 v95, v95
	v_mul_f32_e64 v91, v91, -v151
	v_lshlrev_b32_e32 v106, 16, v147
	v_and_b32_e32 v107, 0xffff0000, v147
	v_pk_mul_f32 v[104:105], v[66:67], v[104:105]
	v_lshlrev_b32_e32 v98, 16, v122
	v_and_b32_e32 v99, 0xffff0000, v122
	v_pk_mul_f32 v[96:97], v[72:73], v[96:97]
	v_mul_f32_e64 v90, v90, -v151
	v_pk_fma_f32 v[102:103], v[104:105], v[102:103], v[106:107]
	v_pk_fma_f32 v[92:93], v[96:97], v[92:93], v[98:99]
	v_exp_f32_e32 v96, v91
	global_store_dwordx4 v[132:133], v[100:103], off offset:528
	v_add_f32_e32 v91, 1.0, v95
	v_rcp_f32_e32 v91, v91
	v_exp_f32_e32 v100, v90
	v_add_f32_e32 v90, 1.0, v94
	v_rcp_f32_e32 v90, v90
	v_add_f32_e32 v95, 1.0, v96
	v_lshlrev_b32_e32 v96, 16, v125
	v_and_b32_e32 v97, 0xffff0000, v125
	v_add_f32_e32 v94, 1.0, v100
	v_pk_mul_f32 v[96:97], v[128:129], v[96:97] op_sel_hi:[0,1]
	v_rcp_f32_e32 v94, v94
	v_rcp_f32_e32 v95, v95
	v_lshlrev_b32_e32 v98, 16, v121
	v_and_b32_e32 v99, 0xffff0000, v121
	v_pk_mul_f32 v[96:97], v[78:79], v[96:97]
	v_mul_f32_e64 v84, v84, -v151
	v_pk_fma_f32 v[90:91], v[96:97], v[90:91], v[98:99]
	v_lshlrev_b32_e32 v96, 16, v127
	v_and_b32_e32 v97, 0xffff0000, v127
	v_pk_mul_f32 v[96:97], v[128:129], v[96:97] op_sel_hi:[0,1]
	v_lshlrev_b32_e32 v98, 16, v123
	v_and_b32_e32 v99, 0xffff0000, v123
	v_pk_mul_f32 v[96:97], v[74:75], v[96:97]
	v_mul_f32_e64 v80, v80, -v151
	v_pk_fma_f32 v[94:95], v[96:97], v[94:95], v[98:99]
	v_lshl_add_u64 v[96:97], v[130:131], 2, s[44:45]
	global_store_dwordx4 v[96:97], v[88:91], off
	v_exp_f32_e32 v84, v84
	v_mul_f32_e64 v85, v85, -v151
	v_exp_f32_e32 v88, v80
	v_exp_f32_e32 v85, v85
	v_mul_f32_e64 v81, v81, -v151
	v_add_f32_e32 v80, 1.0, v84
	v_add_f32_e32 v84, 1.0, v88
	v_exp_f32_e32 v88, v81
	v_add_f32_e32 v81, 1.0, v85
	v_rcp_f32_e32 v80, v80
	v_rcp_f32_e32 v81, v81
	v_add_f32_e32 v85, 1.0, v88
	v_lshlrev_b32_e32 v88, 16, v116
	v_and_b32_e32 v89, 0xffff0000, v116
	v_pk_mul_f32 v[88:89], v[128:129], v[88:89] op_sel_hi:[0,1]
	v_rcp_f32_e32 v84, v84
	v_rcp_f32_e32 v85, v85
	s_waitcnt vmcnt(5)
	v_lshlrev_b32_e32 v90, 16, v112
	v_and_b32_e32 v91, 0xffff0000, v112
	v_pk_mul_f32 v[88:89], v[68:69], v[88:89]
	v_mul_f32_e64 v86, v86, -v151
	v_mul_f32_e64 v87, v87, -v151
	v_pk_fma_f32 v[80:81], v[88:89], v[80:81], v[90:91]
	v_lshlrev_b32_e32 v88, 16, v118
	v_and_b32_e32 v89, 0xffff0000, v118
	v_pk_mul_f32 v[88:89], v[128:129], v[88:89] op_sel_hi:[0,1]
	v_exp_f32_e32 v86, v86
	v_exp_f32_e32 v87, v87
	v_mul_f32_e64 v83, v83, -v151
	v_lshlrev_b32_e32 v90, 16, v114
	v_and_b32_e32 v91, 0xffff0000, v114
	v_pk_mul_f32 v[88:89], v[64:65], v[88:89]
	v_mul_f32_e64 v82, v82, -v151
	v_pk_fma_f32 v[84:85], v[88:89], v[84:85], v[90:91]
	v_exp_f32_e32 v88, v83
	global_store_dwordx4 v[96:97], v[92:95], off offset:16
	v_add_f32_e32 v83, 1.0, v87
	v_rcp_f32_e32 v83, v83
	v_exp_f32_e32 v92, v82
	v_add_f32_e32 v82, 1.0, v86
	v_rcp_f32_e32 v82, v82
	v_add_f32_e32 v87, 1.0, v88
	v_lshlrev_b32_e32 v88, 16, v117
	v_and_b32_e32 v89, 0xffff0000, v117
	v_add_f32_e32 v86, 1.0, v92
	v_pk_mul_f32 v[88:89], v[128:129], v[88:89] op_sel_hi:[0,1]
	v_rcp_f32_e32 v86, v86
	v_rcp_f32_e32 v87, v87
	v_lshlrev_b32_e32 v90, 16, v113
	v_and_b32_e32 v91, 0xffff0000, v113
	v_pk_mul_f32 v[88:89], v[70:71], v[88:89]
	v_add_u32_e32 v98, 0x90, v180
	v_pk_fma_f32 v[82:83], v[88:89], v[82:83], v[90:91]
	v_lshlrev_b32_e32 v88, 16, v119
	v_and_b32_e32 v89, 0xffff0000, v119
	v_pk_mul_f32 v[88:89], v[128:129], v[88:89] op_sel_hi:[0,1]
	v_lshlrev_b32_e32 v90, 16, v115
	v_and_b32_e32 v91, 0xffff0000, v115
	v_pk_mul_f32 v[88:89], v[66:67], v[88:89]
	v_ashrrev_i32_e32 v99, 31, v98
	v_pk_fma_f32 v[86:87], v[88:89], v[86:87], v[90:91]
	global_store_dwordx4 v[96:97], v[80:83], off offset:512
	global_store_dwordx4 v[96:97], v[84:87], off offset:528
	v_add_u32_e32 v96, 0x80, v180
	v_ashrrev_i32_e32 v97, 31, v96
	v_lshlrev_b64 v[84:85], 4, v[96:97]
	v_lshl_add_u64 v[80:81], s[8:9], 0, v[84:85]
	global_load_dwordx4 v[80:83], v[80:81], off
	v_lshl_add_u64 v[84:85], s[10:11], 0, v[84:85]
	global_load_dwordx4 v[84:87], v[84:85], off
	v_lshlrev_b64 v[92:93], 4, v[98:99]
	v_lshl_add_u64 v[88:89], s[8:9], 0, v[92:93]
	global_load_dwordx4 v[88:91], v[88:89], off
	v_lshl_add_u64 v[92:93], s[10:11], 0, v[92:93]
	global_load_dwordx4 v[92:95], v[92:93], off
	v_lshlrev_b64 v[96:97], 10, v[96:97]
	v_lshl_add_u64 v[116:117], v[96:97], 0, v[182:183]
	v_lshlrev_b64 v[96:97], 1, v[116:117]
	v_lshl_add_u64 v[108:109], s[62:63], 0, v[96:97]
	global_load_dwordx4 v[100:103], v[108:109], off
	v_lshl_add_u64 v[96:97], s[60:61], 0, v[96:97]
	global_load_dwordx4 v[104:107], v[96:97], off
	s_waitcnt vmcnt(5)
	v_mov_b32_e32 v110, v81
	v_mov_b32_e32 v111, v82
	v_mov_b32_e32 v81, v83
	v_pk_add_f32 v[80:81], v[110:111], v[80:81]
	global_load_dwordx4 v[108:111], v[108:109], off offset:256
	s_nop 0
	global_load_dwordx4 v[112:115], v[96:97], off offset:256
	v_add_f32_e32 v80, v80, v81
	v_fmamk_f32 v82, v80, 0x3a800000, v192
	s_waitcnt vmcnt(6)
	v_mov_b32_e32 v80, v85
	v_mov_b32_e32 v81, v86
	v_mov_b32_e32 v85, v87
	v_pk_add_f32 v[80:81], v[80:81], v[84:85]
	v_rsq_f32_e32 v97, v82
	s_nop 0
	v_mul_f32_e32 v97, 0x3fb8aa3b, v97
	v_add_f32_e32 v80, v80, v81
	v_fmamk_f32 v80, v80, 0x3a800000, v192
	v_rsq_f32_e32 v118, v80
	v_lshlrev_b64 v[80:81], 10, v[98:99]
	v_lshl_add_u64 v[98:99], v[80:81], 0, v[182:183]
	s_waitcnt vmcnt(5)
	v_mov_b32_e32 v80, v89
	v_mov_b32_e32 v81, v90
	v_mov_b32_e32 v89, v91
	v_pk_add_f32 v[80:81], v[80:81], v[88:89]
	v_mul_f32_e64 v60, v60, -v97
	v_add_f32_e32 v80, v80, v81
	v_fmamk_f32 v119, v80, 0x3a800000, v192
	s_waitcnt vmcnt(4)
	v_mov_b32_e32 v80, v93
	v_mov_b32_e32 v81, v94
	v_mov_b32_e32 v93, v95
	v_pk_add_f32 v[80:81], v[80:81], v[92:93]
	v_mul_f32_e64 v56, v56, -v97
	v_add_f32_e32 v80, v80, v81
	v_fmamk_f32 v80, v80, 0x3a800000, v192
	v_rsq_f32_e32 v96, v80
	v_lshlrev_b64 v[80:81], 1, v[98:99]
	v_lshl_add_u64 v[82:83], s[62:63], 0, v[80:81]
	v_lshl_add_u64 v[80:81], s[60:61], 0, v[80:81]
	global_load_dwordx4 v[92:95], v[82:83], off
	global_load_dwordx4 v[84:87], v[82:83], off offset:256
	global_load_dwordx4 v[88:91], v[80:81], off
	s_nop 0
	global_load_dwordx4 v[80:83], v[80:81], off offset:256
	v_exp_f32_e32 v60, v60
	v_exp_f32_e32 v120, v56
	v_mul_f32_e64 v61, v61, -v97
	v_mul_f32_e64 v57, v57, -v97
	v_add_f32_e32 v56, 1.0, v60
	v_add_f32_e32 v60, 1.0, v120
	v_exp_f32_e32 v61, v61
	v_exp_f32_e32 v120, v57
	v_mul_f32_e64 v62, v62, -v97
	v_mul_f32_e64 v58, v58, -v97
	v_add_f32_e32 v57, 1.0, v61
	v_add_f32_e32 v61, 1.0, v120
	s_waitcnt vmcnt(7)
	v_lshlrev_b32_e32 v120, 16, v100
	v_and_b32_e32 v121, 0xffff0000, v100
	v_exp_f32_e32 v62, v62
	v_exp_f32_e32 v100, v58
	v_mul_f32_e64 v63, v63, -v97
	v_exp_f32_e32 v63, v63
	v_mul_f32_e64 v59, v59, -v97
	v_add_f32_e32 v58, 1.0, v62
	v_add_f32_e32 v62, 1.0, v100
	v_exp_f32_e32 v100, v59
	v_rsq_f32_e32 v119, v119
	s_nop 0
	v_mul_f32_e32 v119, 0x3fb8aa3b, v119
	v_add_f32_e32 v59, 1.0, v63
	v_rcp_f32_e32 v58, v58
	v_rcp_f32_e32 v59, v59
	v_add_f32_e32 v63, 1.0, v100
	v_lshlrev_b32_e32 v100, 16, v101
	v_and_b32_e32 v101, 0xffff0000, v101
	v_rcp_f32_e32 v56, v56
	v_rcp_f32_e32 v57, v57
	v_pk_mul_f32 v[100:101], v[118:119], v[100:101] op_sel_hi:[0,1]
	s_waitcnt vmcnt(6)
	v_lshlrev_b32_e32 v122, 16, v104
	v_and_b32_e32 v123, 0xffff0000, v104
	v_rcp_f32_e32 v62, v62
	v_rcp_f32_e32 v63, v63
	v_lshlrev_b32_e32 v104, 16, v105
	v_and_b32_e32 v105, 0xffff0000, v105
	v_pk_mul_f32 v[100:101], v[78:79], v[100:101]
	v_pk_mul_f32 v[120:121], v[118:119], v[120:121] op_sel_hi:[0,1]
	v_pk_fma_f32 v[58:59], v[100:101], v[58:59], v[104:105]
	v_lshlrev_b32_e32 v100, 16, v103
	v_and_b32_e32 v101, 0xffff0000, v103
	v_pk_mul_f32 v[120:121], v[76:77], v[120:121]
	v_pk_mul_f32 v[100:101], v[118:119], v[100:101] op_sel_hi:[0,1]
	v_pk_fma_f32 v[56:57], v[120:121], v[56:57], v[122:123]
	v_lshlrev_b32_e32 v120, 16, v102
	v_and_b32_e32 v121, 0xffff0000, v102
	v_lshlrev_b32_e32 v102, 16, v107
	v_and_b32_e32 v103, 0xffff0000, v107
	v_pk_mul_f32 v[100:101], v[74:75], v[100:101]
	v_mul_f32_e64 v52, v52, -v97
	v_mul_f32_e64 v48, v48, -v97
	v_pk_fma_f32 v[62:63], v[100:101], v[62:63], v[102:103]
	v_lshl_add_u64 v[100:101], v[116:117], 2, s[44:45]
	global_store_dwordx4 v[100:101], v[56:59], off
	v_exp_f32_e32 v52, v52
	v_mul_f32_e64 v53, v53, -v97
	v_exp_f32_e32 v56, v48
	v_exp_f32_e32 v53, v53
	v_mul_f32_e64 v49, v49, -v97
	v_add_f32_e32 v48, 1.0, v52
	v_add_f32_e32 v52, 1.0, v56
	v_exp_f32_e32 v56, v49
	v_add_f32_e32 v49, 1.0, v53
	v_rcp_f32_e32 v48, v48
	v_rcp_f32_e32 v49, v49
	v_add_f32_e32 v53, 1.0, v56
	s_waitcnt vmcnt(6)
	v_lshlrev_b32_e32 v56, 16, v108
	v_and_b32_e32 v57, 0xffff0000, v108
	v_pk_mul_f32 v[56:57], v[118:119], v[56:57] op_sel_hi:[0,1]
	v_rcp_f32_e32 v52, v52
	v_rcp_f32_e32 v53, v53
	s_waitcnt vmcnt(5)
	v_lshlrev_b32_e32 v58, 16, v112
	v_and_b32_e32 v59, 0xffff0000, v112
	v_pk_mul_f32 v[56:57], v[68:69], v[56:57]
	v_mul_f32_e64 v54, v54, -v97
	v_mul_f32_e64 v55, v55, -v97
	v_rcp_f32_e32 v60, v60
	v_rcp_f32_e32 v61, v61
	v_pk_fma_f32 v[48:49], v[56:57], v[48:49], v[58:59]
	v_lshlrev_b32_e32 v56, 16, v110
	v_and_b32_e32 v57, 0xffff0000, v110
	v_pk_mul_f32 v[56:57], v[118:119], v[56:57] op_sel_hi:[0,1]
	v_exp_f32_e32 v54, v54
	v_exp_f32_e32 v55, v55
	v_mul_f32_e64 v51, v51, -v97
	v_pk_mul_f32 v[120:121], v[118:119], v[120:121] op_sel_hi:[0,1]
	v_lshlrev_b32_e32 v58, 16, v114
	v_and_b32_e32 v59, 0xffff0000, v114
	v_pk_mul_f32 v[56:57], v[64:65], v[56:57]
	v_lshlrev_b32_e32 v122, 16, v106
	v_and_b32_e32 v123, 0xffff0000, v106
	v_pk_mul_f32 v[120:121], v[72:73], v[120:121]
	v_mul_f32_e64 v50, v50, -v97
	v_pk_fma_f32 v[52:53], v[56:57], v[52:53], v[58:59]
	v_exp_f32_e32 v56, v51
	v_pk_fma_f32 v[60:61], v[120:121], v[60:61], v[122:123]
	global_store_dwordx4 v[100:101], v[60:63], off offset:16
	v_add_f32_e32 v51, 1.0, v55
	v_rcp_f32_e32 v51, v51
	v_exp_f32_e32 v60, v50
	v_add_f32_e32 v50, 1.0, v54
	v_rcp_f32_e32 v50, v50
	v_add_f32_e32 v55, 1.0, v56
	v_lshlrev_b32_e32 v56, 16, v109
	v_and_b32_e32 v57, 0xffff0000, v109
	v_pk_mul_f32 v[56:57], v[118:119], v[56:57] op_sel_hi:[0,1]
	v_lshlrev_b32_e32 v58, 16, v113
	v_and_b32_e32 v59, 0xffff0000, v113
	v_pk_mul_f32 v[56:57], v[70:71], v[56:57]
	v_mul_f32_e64 v44, v44, -v119
	v_mul_f32_e64 v40, v40, -v119
	v_pk_fma_f32 v[50:51], v[56:57], v[50:51], v[58:59]
	global_store_dwordx4 v[100:101], v[48:51], off offset:512
	v_exp_f32_e32 v44, v44
	v_mul_f32_e64 v45, v45, -v119
	v_exp_f32_e32 v48, v40
	v_exp_f32_e32 v45, v45
	v_mul_f32_e64 v41, v41, -v119
	v_add_f32_e32 v40, 1.0, v44
	v_add_f32_e32 v44, 1.0, v48
	v_exp_f32_e32 v48, v41
	v_add_f32_e32 v41, 1.0, v45
	v_rcp_f32_e32 v40, v40
	v_rcp_f32_e32 v41, v41
	v_add_f32_e32 v45, 1.0, v48
	s_waitcnt vmcnt(6)
	v_lshlrev_b32_e32 v48, 16, v92
	v_and_b32_e32 v49, 0xffff0000, v92
	v_add_f32_e32 v54, 1.0, v60
	v_pk_mul_f32 v[48:49], v[96:97], v[48:49] op_sel_hi:[0,1]
	v_rcp_f32_e32 v54, v54
	v_rcp_f32_e32 v55, v55
	v_rcp_f32_e32 v44, v44
	v_rcp_f32_e32 v45, v45
	s_waitcnt vmcnt(4)
	v_lshlrev_b32_e32 v50, 16, v88
	v_and_b32_e32 v51, 0xffff0000, v88
	v_pk_mul_f32 v[48:49], v[76:77], v[48:49]
	v_mul_f32_e64 v46, v46, -v119
	v_mul_f32_e64 v47, v47, -v119
	v_lshlrev_b32_e32 v56, 16, v111
	v_and_b32_e32 v57, 0xffff0000, v111
	v_pk_fma_f32 v[40:41], v[48:49], v[40:41], v[50:51]
	v_lshlrev_b32_e32 v48, 16, v94
	v_and_b32_e32 v49, 0xffff0000, v94
	v_pk_mul_f32 v[56:57], v[118:119], v[56:57] op_sel_hi:[0,1]
	v_pk_mul_f32 v[48:49], v[96:97], v[48:49] op_sel_hi:[0,1]
	v_exp_f32_e32 v46, v46
	v_exp_f32_e32 v47, v47
	v_mul_f32_e64 v43, v43, -v119
	v_lshlrev_b32_e32 v58, 16, v115
	v_and_b32_e32 v59, 0xffff0000, v115
	v_pk_mul_f32 v[56:57], v[66:67], v[56:57]
	v_lshlrev_b32_e32 v50, 16, v90
	v_and_b32_e32 v51, 0xffff0000, v90
	v_pk_mul_f32 v[48:49], v[72:73], v[48:49]
	v_mul_f32_e64 v42, v42, -v119
	v_pk_fma_f32 v[54:55], v[56:57], v[54:55], v[58:59]
	v_pk_fma_f32 v[44:45], v[48:49], v[44:45], v[50:51]
	v_exp_f32_e32 v48, v43
	global_store_dwordx4 v[100:101], v[52:55], off offset:528
	v_add_f32_e32 v43, 1.0, v47
	v_rcp_f32_e32 v43, v43
	v_exp_f32_e32 v52, v42
	v_add_f32_e32 v42, 1.0, v46
	v_rcp_f32_e32 v42, v42
	v_add_f32_e32 v47, 1.0, v48
	v_lshlrev_b32_e32 v48, 16, v93
	v_and_b32_e32 v49, 0xffff0000, v93
	v_add_f32_e32 v46, 1.0, v52
	v_pk_mul_f32 v[48:49], v[96:97], v[48:49] op_sel_hi:[0,1]
	v_rcp_f32_e32 v46, v46
	v_rcp_f32_e32 v47, v47
	v_lshlrev_b32_e32 v50, 16, v89
	v_and_b32_e32 v51, 0xffff0000, v89
	v_pk_mul_f32 v[48:49], v[78:79], v[48:49]
	v_mul_f32_e64 v36, v36, -v119
	v_pk_fma_f32 v[42:43], v[48:49], v[42:43], v[50:51]
	v_lshlrev_b32_e32 v48, 16, v95
	v_and_b32_e32 v49, 0xffff0000, v95
	v_pk_mul_f32 v[48:49], v[96:97], v[48:49] op_sel_hi:[0,1]
	v_lshlrev_b32_e32 v50, 16, v91
	v_and_b32_e32 v51, 0xffff0000, v91
	v_pk_mul_f32 v[48:49], v[74:75], v[48:49]
	v_mul_f32_e64 v32, v32, -v119
	v_pk_fma_f32 v[46:47], v[48:49], v[46:47], v[50:51]
	v_lshl_add_u64 v[48:49], v[98:99], 2, s[44:45]
	global_store_dwordx4 v[48:49], v[40:43], off
	v_exp_f32_e32 v36, v36
	v_mul_f32_e64 v37, v37, -v119
	v_exp_f32_e32 v40, v32
	v_exp_f32_e32 v37, v37
	v_mul_f32_e64 v33, v33, -v119
	v_add_f32_e32 v32, 1.0, v36
	v_add_f32_e32 v36, 1.0, v40
	v_exp_f32_e32 v40, v33
	v_add_f32_e32 v33, 1.0, v37
	v_rcp_f32_e32 v32, v32
	v_rcp_f32_e32 v33, v33
	v_add_f32_e32 v37, 1.0, v40
	v_lshlrev_b32_e32 v40, 16, v84
	v_and_b32_e32 v41, 0xffff0000, v84
	v_pk_mul_f32 v[40:41], v[96:97], v[40:41] op_sel_hi:[0,1]
	v_rcp_f32_e32 v36, v36
	v_rcp_f32_e32 v37, v37
	s_waitcnt vmcnt(5)
	v_lshlrev_b32_e32 v42, 16, v80
	v_and_b32_e32 v43, 0xffff0000, v80
	v_pk_mul_f32 v[40:41], v[68:69], v[40:41]
	v_mul_f32_e64 v38, v38, -v119
	v_mul_f32_e64 v39, v39, -v119
	v_pk_fma_f32 v[32:33], v[40:41], v[32:33], v[42:43]
	v_lshlrev_b32_e32 v40, 16, v86
	v_and_b32_e32 v41, 0xffff0000, v86
	v_pk_mul_f32 v[40:41], v[96:97], v[40:41] op_sel_hi:[0,1]
	v_exp_f32_e32 v38, v38
	v_exp_f32_e32 v39, v39
	v_mul_f32_e64 v35, v35, -v119
	v_lshlrev_b32_e32 v42, 16, v82
	v_and_b32_e32 v43, 0xffff0000, v82
	v_pk_mul_f32 v[40:41], v[64:65], v[40:41]
	v_mul_f32_e64 v34, v34, -v119
	v_pk_fma_f32 v[36:37], v[40:41], v[36:37], v[42:43]
	v_exp_f32_e32 v40, v35
	global_store_dwordx4 v[48:49], v[44:47], off offset:16
	v_add_f32_e32 v35, 1.0, v39
	v_rcp_f32_e32 v35, v35
	v_exp_f32_e32 v44, v34
	v_add_f32_e32 v34, 1.0, v38
	v_rcp_f32_e32 v34, v34
	v_add_f32_e32 v39, 1.0, v40
	v_lshlrev_b32_e32 v40, 16, v85
	v_and_b32_e32 v41, 0xffff0000, v85
	v_add_f32_e32 v38, 1.0, v44
	v_pk_mul_f32 v[40:41], v[96:97], v[40:41] op_sel_hi:[0,1]
	v_rcp_f32_e32 v38, v38
	v_rcp_f32_e32 v39, v39
	v_lshlrev_b32_e32 v42, 16, v81
	v_and_b32_e32 v43, 0xffff0000, v81
	v_pk_mul_f32 v[40:41], v[70:71], v[40:41]
	v_add_u32_e32 v50, 0xb0, v180
	v_pk_fma_f32 v[34:35], v[40:41], v[34:35], v[42:43]
	v_lshlrev_b32_e32 v40, 16, v87
	v_and_b32_e32 v41, 0xffff0000, v87
	v_pk_mul_f32 v[40:41], v[96:97], v[40:41] op_sel_hi:[0,1]
	v_lshlrev_b32_e32 v42, 16, v83
	v_and_b32_e32 v43, 0xffff0000, v83
	v_pk_mul_f32 v[40:41], v[66:67], v[40:41]
	v_ashrrev_i32_e32 v51, 31, v50
	v_pk_fma_f32 v[38:39], v[40:41], v[38:39], v[42:43]
	global_store_dwordx4 v[48:49], v[32:35], off offset:512
	global_store_dwordx4 v[48:49], v[36:39], off offset:528
	v_add_u32_e32 v48, 0xa0, v180
	v_ashrrev_i32_e32 v49, 31, v48
	v_lshlrev_b64 v[36:37], 4, v[48:49]
	v_lshl_add_u64 v[32:33], s[8:9], 0, v[36:37]
	global_load_dwordx4 v[32:35], v[32:33], off
	v_lshl_add_u64 v[36:37], s[10:11], 0, v[36:37]
	global_load_dwordx4 v[36:39], v[36:37], off
	v_lshlrev_b64 v[44:45], 4, v[50:51]
	v_lshl_add_u64 v[40:41], s[8:9], 0, v[44:45]
	global_load_dwordx4 v[40:43], v[40:41], off
	v_lshl_add_u64 v[44:45], s[10:11], 0, v[44:45]
	global_load_dwordx4 v[44:47], v[44:45], off
	v_lshlrev_b64 v[48:49], 10, v[48:49]
	v_lshl_add_u64 v[84:85], v[48:49], 0, v[182:183]
	v_lshlrev_b64 v[48:49], 1, v[84:85]
	v_lshl_add_u64 v[86:87], s[62:63], 0, v[48:49]
	global_load_dwordx4 v[52:55], v[86:87], off
	v_lshl_add_u64 v[48:49], s[60:61], 0, v[48:49]
	global_load_dwordx4 v[56:59], v[48:49], off
	s_waitcnt vmcnt(5)
	v_mov_b32_e32 v60, v33
	v_mov_b32_e32 v61, v34
	v_mov_b32_e32 v33, v35
	v_pk_add_f32 v[32:33], v[60:61], v[32:33]
	global_load_dwordx4 v[60:63], v[86:87], off offset:256
	global_load_dwordx4 v[80:83], v[48:49], off offset:256
	v_add_f32_e32 v32, v32, v33
	v_fmamk_f32 v34, v32, 0x3a800000, v192
	s_waitcnt vmcnt(6)
	v_mov_b32_e32 v32, v37
	v_mov_b32_e32 v33, v38
	v_mov_b32_e32 v37, v39
	v_pk_add_f32 v[32:33], v[32:33], v[36:37]
	v_rsq_f32_e32 v49, v34
	s_nop 0
	v_mul_f32_e32 v49, 0x3fb8aa3b, v49
	v_add_f32_e32 v32, v32, v33
	v_fmamk_f32 v32, v32, 0x3a800000, v192
	v_rsq_f32_e32 v88, v32
	v_lshlrev_b64 v[32:33], 10, v[50:51]
	v_lshl_add_u64 v[50:51], v[32:33], 0, v[182:183]
	s_waitcnt vmcnt(5)
	v_mov_b32_e32 v32, v41
	v_mov_b32_e32 v33, v42
	v_mov_b32_e32 v41, v43
	v_pk_add_f32 v[32:33], v[32:33], v[40:41]
	v_mul_f32_e64 v28, v28, -v49
	v_add_f32_e32 v32, v32, v33
	v_fmamk_f32 v89, v32, 0x3a800000, v192
	s_waitcnt vmcnt(4)
	v_mov_b32_e32 v32, v45
	v_mov_b32_e32 v33, v46
	v_mov_b32_e32 v45, v47
	v_pk_add_f32 v[32:33], v[32:33], v[44:45]
	v_mul_f32_e64 v24, v24, -v49
	v_add_f32_e32 v32, v32, v33
	v_fmamk_f32 v32, v32, 0x3a800000, v192
	v_rsq_f32_e32 v48, v32
	v_lshlrev_b64 v[32:33], 1, v[50:51]
	v_lshl_add_u64 v[86:87], s[62:63], 0, v[32:33]
	v_lshl_add_u64 v[90:91], s[60:61], 0, v[32:33]
	global_load_dwordx4 v[44:47], v[86:87], off
	global_load_dwordx4 v[36:39], v[86:87], off offset:256
	global_load_dwordx4 v[40:43], v[90:91], off
	global_load_dwordx4 v[32:35], v[90:91], off offset:256
	v_exp_f32_e32 v28, v28
	v_exp_f32_e32 v86, v24
	v_mul_f32_e64 v29, v29, -v49
	v_mul_f32_e64 v25, v25, -v49
	v_add_f32_e32 v24, 1.0, v28
	v_add_f32_e32 v28, 1.0, v86
	v_exp_f32_e32 v29, v29
	v_exp_f32_e32 v86, v25
	v_mul_f32_e64 v30, v30, -v49
	v_mul_f32_e64 v26, v26, -v49
	v_add_f32_e32 v25, 1.0, v29
	v_add_f32_e32 v29, 1.0, v86
	s_waitcnt vmcnt(7)
	v_lshlrev_b32_e32 v86, 16, v52
	v_and_b32_e32 v87, 0xffff0000, v52
	v_exp_f32_e32 v30, v30
	v_exp_f32_e32 v52, v26
	v_mul_f32_e64 v31, v31, -v49
	v_exp_f32_e32 v31, v31
	v_mul_f32_e64 v27, v27, -v49
	v_add_f32_e32 v26, 1.0, v30
	v_add_f32_e32 v30, 1.0, v52
	v_exp_f32_e32 v52, v27
	v_rsq_f32_e32 v89, v89
	s_nop 0
	v_mul_f32_e32 v89, 0x3fb8aa3b, v89
	v_add_f32_e32 v27, 1.0, v31
	v_rcp_f32_e32 v26, v26
	v_rcp_f32_e32 v27, v27
	v_add_f32_e32 v31, 1.0, v52
	v_lshlrev_b32_e32 v52, 16, v53
	v_and_b32_e32 v53, 0xffff0000, v53
	v_rcp_f32_e32 v24, v24
	v_rcp_f32_e32 v25, v25
	v_pk_mul_f32 v[52:53], v[88:89], v[52:53] op_sel_hi:[0,1]
	s_waitcnt vmcnt(6)
	v_lshlrev_b32_e32 v90, 16, v56
	v_and_b32_e32 v91, 0xffff0000, v56
	v_rcp_f32_e32 v30, v30
	v_rcp_f32_e32 v31, v31
	v_lshlrev_b32_e32 v56, 16, v57
	v_and_b32_e32 v57, 0xffff0000, v57
	v_pk_mul_f32 v[52:53], v[78:79], v[52:53]
	v_pk_mul_f32 v[86:87], v[88:89], v[86:87] op_sel_hi:[0,1]
	v_pk_fma_f32 v[26:27], v[52:53], v[26:27], v[56:57]
	v_lshlrev_b32_e32 v52, 16, v55
	v_and_b32_e32 v53, 0xffff0000, v55
	v_pk_mul_f32 v[86:87], v[76:77], v[86:87]
	v_pk_mul_f32 v[52:53], v[88:89], v[52:53] op_sel_hi:[0,1]
	v_pk_fma_f32 v[24:25], v[86:87], v[24:25], v[90:91]
	v_lshlrev_b32_e32 v86, 16, v54
	v_and_b32_e32 v87, 0xffff0000, v54
	v_lshlrev_b32_e32 v54, 16, v59
	v_and_b32_e32 v55, 0xffff0000, v59
	v_pk_mul_f32 v[52:53], v[74:75], v[52:53]
	v_mul_f32_e64 v20, v20, -v49
	v_mul_f32_e64 v16, v16, -v49
	v_pk_fma_f32 v[30:31], v[52:53], v[30:31], v[54:55]
	v_lshl_add_u64 v[52:53], v[84:85], 2, s[44:45]
	global_store_dwordx4 v[52:53], v[24:27], off
	v_exp_f32_e32 v20, v20
	v_mul_f32_e64 v21, v21, -v49
	v_exp_f32_e32 v24, v16
	v_exp_f32_e32 v21, v21
	v_mul_f32_e64 v17, v17, -v49
	v_add_f32_e32 v16, 1.0, v20
	v_add_f32_e32 v20, 1.0, v24
	v_exp_f32_e32 v24, v17
	v_add_f32_e32 v17, 1.0, v21
	v_rcp_f32_e32 v16, v16
	v_rcp_f32_e32 v17, v17
	v_add_f32_e32 v21, 1.0, v24
	s_waitcnt vmcnt(6)
	v_lshlrev_b32_e32 v24, 16, v60
	v_and_b32_e32 v25, 0xffff0000, v60
	v_pk_mul_f32 v[24:25], v[88:89], v[24:25] op_sel_hi:[0,1]
	v_rcp_f32_e32 v20, v20
	v_rcp_f32_e32 v21, v21
	s_waitcnt vmcnt(5)
	v_lshlrev_b32_e32 v26, 16, v80
	v_and_b32_e32 v27, 0xffff0000, v80
	v_pk_mul_f32 v[24:25], v[68:69], v[24:25]
	v_mul_f32_e64 v22, v22, -v49
	v_mul_f32_e64 v23, v23, -v49
	v_rcp_f32_e32 v28, v28
	v_rcp_f32_e32 v29, v29
	v_pk_fma_f32 v[16:17], v[24:25], v[16:17], v[26:27]
	v_lshlrev_b32_e32 v24, 16, v62
	v_and_b32_e32 v25, 0xffff0000, v62
	v_pk_mul_f32 v[24:25], v[88:89], v[24:25] op_sel_hi:[0,1]
	v_exp_f32_e32 v22, v22
	v_exp_f32_e32 v23, v23
	v_mul_f32_e64 v19, v19, -v49
	v_pk_mul_f32 v[86:87], v[88:89], v[86:87] op_sel_hi:[0,1]
	v_lshlrev_b32_e32 v26, 16, v82
	v_and_b32_e32 v27, 0xffff0000, v82
	v_pk_mul_f32 v[24:25], v[64:65], v[24:25]
	v_lshlrev_b32_e32 v90, 16, v58
	v_and_b32_e32 v91, 0xffff0000, v58
	v_pk_mul_f32 v[86:87], v[72:73], v[86:87]
	v_mul_f32_e64 v18, v18, -v49
	v_pk_fma_f32 v[20:21], v[24:25], v[20:21], v[26:27]
	v_exp_f32_e32 v24, v19
	v_pk_fma_f32 v[28:29], v[86:87], v[28:29], v[90:91]
	global_store_dwordx4 v[52:53], v[28:31], off offset:16
	v_add_f32_e32 v19, 1.0, v23
	v_rcp_f32_e32 v19, v19
	v_exp_f32_e32 v28, v18
	v_add_f32_e32 v18, 1.0, v22
	v_rcp_f32_e32 v18, v18
	v_add_f32_e32 v23, 1.0, v24
	v_lshlrev_b32_e32 v24, 16, v61
	v_and_b32_e32 v25, 0xffff0000, v61
	v_pk_mul_f32 v[24:25], v[88:89], v[24:25] op_sel_hi:[0,1]
	v_lshlrev_b32_e32 v26, 16, v81
	v_and_b32_e32 v27, 0xffff0000, v81
	v_pk_mul_f32 v[24:25], v[70:71], v[24:25]
	v_mul_f32_e64 v12, v12, -v89
	v_mul_f32_e64 v8, v8, -v89
	v_pk_fma_f32 v[18:19], v[24:25], v[18:19], v[26:27]
	global_store_dwordx4 v[52:53], v[16:19], off offset:512
	v_exp_f32_e32 v12, v12
	v_mul_f32_e64 v13, v13, -v89
	v_exp_f32_e32 v16, v8
	v_exp_f32_e32 v13, v13
	v_mul_f32_e64 v9, v9, -v89
	v_add_f32_e32 v8, 1.0, v12
	v_add_f32_e32 v12, 1.0, v16
	v_exp_f32_e32 v16, v9
	v_add_f32_e32 v9, 1.0, v13
	v_rcp_f32_e32 v8, v8
	v_rcp_f32_e32 v9, v9
	v_add_f32_e32 v13, 1.0, v16
	s_waitcnt vmcnt(6)
	v_lshlrev_b32_e32 v16, 16, v44
	v_and_b32_e32 v17, 0xffff0000, v44
	v_add_f32_e32 v22, 1.0, v28
	v_pk_mul_f32 v[16:17], v[48:49], v[16:17] op_sel_hi:[0,1]
	v_rcp_f32_e32 v22, v22
	v_rcp_f32_e32 v23, v23
	v_rcp_f32_e32 v12, v12
	v_rcp_f32_e32 v13, v13
	s_waitcnt vmcnt(4)
	v_lshlrev_b32_e32 v18, 16, v40
	v_and_b32_e32 v19, 0xffff0000, v40
	v_pk_mul_f32 v[16:17], v[76:77], v[16:17]
	v_mul_f32_e64 v14, v14, -v89
	v_mul_f32_e64 v15, v15, -v89
	v_lshlrev_b32_e32 v24, 16, v63
	v_and_b32_e32 v25, 0xffff0000, v63
	v_pk_fma_f32 v[8:9], v[16:17], v[8:9], v[18:19]
	v_lshlrev_b32_e32 v16, 16, v46
	v_and_b32_e32 v17, 0xffff0000, v46
	v_pk_mul_f32 v[24:25], v[88:89], v[24:25] op_sel_hi:[0,1]
	v_pk_mul_f32 v[16:17], v[48:49], v[16:17] op_sel_hi:[0,1]
	v_exp_f32_e32 v14, v14
	v_exp_f32_e32 v15, v15
	v_mul_f32_e64 v11, v11, -v89
	v_lshlrev_b32_e32 v26, 16, v83
	v_and_b32_e32 v27, 0xffff0000, v83
	v_pk_mul_f32 v[24:25], v[66:67], v[24:25]
	v_lshlrev_b32_e32 v18, 16, v42
	v_and_b32_e32 v19, 0xffff0000, v42
	v_pk_mul_f32 v[16:17], v[72:73], v[16:17]
	v_mul_f32_e64 v10, v10, -v89
	v_pk_fma_f32 v[22:23], v[24:25], v[22:23], v[26:27]
	v_pk_fma_f32 v[12:13], v[16:17], v[12:13], v[18:19]
	v_exp_f32_e32 v16, v11
	global_store_dwordx4 v[52:53], v[20:23], off offset:528
	v_add_f32_e32 v11, 1.0, v15
	v_rcp_f32_e32 v11, v11
	v_exp_f32_e32 v20, v10
	v_add_f32_e32 v10, 1.0, v14
	v_rcp_f32_e32 v10, v10
	v_add_f32_e32 v15, 1.0, v16
	v_lshlrev_b32_e32 v16, 16, v45
	v_and_b32_e32 v17, 0xffff0000, v45
	v_add_f32_e32 v14, 1.0, v20
	v_pk_mul_f32 v[16:17], v[48:49], v[16:17] op_sel_hi:[0,1]
	v_rcp_f32_e32 v14, v14
	v_rcp_f32_e32 v15, v15
	v_lshlrev_b32_e32 v18, 16, v41
	v_and_b32_e32 v19, 0xffff0000, v41
	v_pk_mul_f32 v[16:17], v[78:79], v[16:17]
	v_mul_f32_e64 v4, v4, -v89
	v_pk_fma_f32 v[10:11], v[16:17], v[10:11], v[18:19]
	v_lshlrev_b32_e32 v16, 16, v47
	v_and_b32_e32 v17, 0xffff0000, v47
	v_pk_mul_f32 v[16:17], v[48:49], v[16:17] op_sel_hi:[0,1]
	v_lshlrev_b32_e32 v18, 16, v43
	v_and_b32_e32 v19, 0xffff0000, v43
	v_pk_mul_f32 v[16:17], v[74:75], v[16:17]
	v_mul_f32_e64 v0, v0, -v89
	v_pk_fma_f32 v[14:15], v[16:17], v[14:15], v[18:19]
	v_lshl_add_u64 v[16:17], v[50:51], 2, s[44:45]
	global_store_dwordx4 v[16:17], v[8:11], off
	v_exp_f32_e32 v4, v4
	v_mul_f32_e64 v5, v5, -v89
	v_exp_f32_e32 v8, v0
	v_exp_f32_e32 v5, v5
	v_mul_f32_e64 v1, v1, -v89
	v_add_f32_e32 v0, 1.0, v4
	v_add_f32_e32 v4, 1.0, v8
	v_exp_f32_e32 v8, v1
	v_add_f32_e32 v1, 1.0, v5
	v_rcp_f32_e32 v0, v0
	v_rcp_f32_e32 v1, v1
	v_add_f32_e32 v5, 1.0, v8
	v_lshlrev_b32_e32 v8, 16, v36
	v_and_b32_e32 v9, 0xffff0000, v36
	v_pk_mul_f32 v[8:9], v[48:49], v[8:9] op_sel_hi:[0,1]
	v_rcp_f32_e32 v4, v4
	v_rcp_f32_e32 v5, v5
	s_waitcnt vmcnt(5)
	v_lshlrev_b32_e32 v10, 16, v32
	v_and_b32_e32 v11, 0xffff0000, v32
	v_pk_mul_f32 v[8:9], v[68:69], v[8:9]
	v_mul_f32_e64 v6, v6, -v89
	v_mul_f32_e64 v7, v7, -v89
	v_pk_fma_f32 v[0:1], v[8:9], v[0:1], v[10:11]
	v_lshlrev_b32_e32 v8, 16, v38
	v_and_b32_e32 v9, 0xffff0000, v38
	v_pk_mul_f32 v[8:9], v[48:49], v[8:9] op_sel_hi:[0,1]
	v_exp_f32_e32 v6, v6
	v_exp_f32_e32 v7, v7
	v_mul_f32_e64 v3, v3, -v89
	v_lshlrev_b32_e32 v10, 16, v34
	v_and_b32_e32 v11, 0xffff0000, v34
	v_pk_mul_f32 v[8:9], v[64:65], v[8:9]
	v_mul_f32_e64 v2, v2, -v89
	v_pk_fma_f32 v[4:5], v[8:9], v[4:5], v[10:11]
	v_exp_f32_e32 v8, v3
	global_store_dwordx4 v[16:17], v[12:15], off offset:16
	v_add_f32_e32 v3, 1.0, v7
	v_rcp_f32_e32 v3, v3
	v_exp_f32_e32 v12, v2
	v_add_f32_e32 v2, 1.0, v6
	v_rcp_f32_e32 v2, v2
	v_add_f32_e32 v7, 1.0, v8
	v_lshlrev_b32_e32 v8, 16, v37
	v_and_b32_e32 v9, 0xffff0000, v37
	v_add_f32_e32 v6, 1.0, v12
	v_pk_mul_f32 v[8:9], v[48:49], v[8:9] op_sel_hi:[0,1]
	v_rcp_f32_e32 v6, v6
	v_rcp_f32_e32 v7, v7
	v_lshlrev_b32_e32 v10, 16, v33
	v_and_b32_e32 v11, 0xffff0000, v33
	v_pk_mul_f32 v[8:9], v[70:71], v[8:9]
	s_nop 0
	v_pk_fma_f32 v[2:3], v[8:9], v[2:3], v[10:11]
	v_lshlrev_b32_e32 v8, 16, v39
	v_and_b32_e32 v9, 0xffff0000, v39
	v_pk_mul_f32 v[8:9], v[48:49], v[8:9] op_sel_hi:[0,1]
	v_lshlrev_b32_e32 v10, 16, v35
	v_and_b32_e32 v11, 0xffff0000, v35
	v_pk_mul_f32 v[8:9], v[66:67], v[8:9]
	s_nop 0
	v_pk_fma_f32 v[6:7], v[8:9], v[6:7], v[10:11]
	global_store_dwordx4 v[16:17], v[0:3], off offset:512
	global_store_dwordx4 v[16:17], v[4:7], off offset:528
	s_cbranch_vccnz .LBB0_2171
